# conv1r with conversion quota 2 per workgroup in the attention phase
# baseline (speedup 1.0000x reference)
; __device__ __forceinline__ unsigned xb_ld(unsigned* p)              { return __hip_atomic_load(p, __ATOMIC_RELAXED, __HIP_MEMORY_SCOPE_AGENT); }
; __device__ __forceinline__ unsigned xb_add(unsigned* p, unsigned v) { return __hip_atomic_fetch_add(p, v, __ATOMIC_RELAXED, __HIP_MEMORY_SCOPE_AGENT); }
;     ...
;     unsigned ahead = 0xFFFFFFFFu;
;     if (tl == 0 && max_claims > 0) { if (xb_ld(qw) < (unsigned)target) ahead = xb_add(qw, 32u); }
;     for (int nc = 0; nc < max_claims; ++nc) {
;         if (tl == 0) { st[6] = ahead; if (ahead < (unsigned)target && nc + 1 < max_claims) ahead = (ahead + 32u < (unsigned)target) ? xb_add(qw, 32u) : 0xFFFFFFFFu; }
;         __syncthreads();
;         const unsigned base = st[6];
.LBB0_698:
	s_and_saveexec_b64 s[0:1], s[2:3]
	s_cbranch_execz .LBB0_706
	v_readlane_b32 s14, v254, 27
	s_cmp_lt_u32 s30, 1
	v_cmp_gt_u32_e32 vcc, s25, v129
	v_mov_b32_e32 v139, s14
	s_cselect_b64 s[14:15], -1, 0
	s_and_b64 s[16:17], vcc, s[14:15]
	ds_write_b32 v139, v129
	s_and_saveexec_b64 s[14:15], s[16:17]
	s_cbranch_execz .LBB0_705
	v_cmp_gt_u32_e32 vcc, s27, v129
	v_mov_b32_e32 v129, -1
	s_and_saveexec_b64 s[16:17], vcc
	s_cbranch_execz .LBB0_704
	s_mov_b64 s[20:21], exec
	v_mbcnt_lo_u32_b32 v129, s20, 0
	v_mbcnt_hi_u32_b32 v129, s21, v129
	v_cmp_eq_u32_e32 vcc, 0, v129
	s_and_saveexec_b64 s[18:19], vcc
	s_cbranch_execz .LBB0_703
	s_bcnt1_i32_b64 s20, s[20:21]
	s_lshl_b32 s20, s20, 5
	v_mov_b32_e32 v139, s20
	global_atomic_add v139, v193, v139, s[4:5] sc0

; __device__ __forceinline__ unsigned xb_add(unsigned* p, unsigned v) { return __hip_atomic_fetch_add(p, v, __ATOMIC_RELAXED, __HIP_MEMORY_SCOPE_AGENT); }
;     __device__ __forceinline__ unsigned char* ws() const { return *(unsigned char* const __attribute__((address_space(4)))*)(p + 232); }
;     ...
;     for (int nc = 0; nc < max_claims; ++nc) {
;         if (tl == 0) { st[6] = ahead; if (ahead < (unsigned)target && nc + 1 < max_claims) ahead = (ahead + 32u < (unsigned)target) ? xb_add(qw, 32u) : 0xFFFFFFFFu; }
;         __syncthreads();
;         const unsigned base = st[6];
;         if (base < (unsigned)Q_TOTAL) {
;             const int q0 = (int)base + wave; const bool v0 = q0 < Q_TOTAL, v1 = q0 + 8 < Q_TOTAL, v2 = q0 + 16 < Q_TOTAL, v3 = q0 + 24 < Q_TOTAL;
;             float ta[64], tb[64]; CvtDesc da, db;
;             if (v0) { da = conv_expert_desc(a, ws, q0); cvt_load(da, ta, lane); }
;             if (v1) { db = conv_expert_desc(a, ws, q0 + 8); cvt_load(db, tb, lane); }
;             if (v0) cvt_finish(da, ta, scr, lane);
;             if (v2) { da = conv_expert_desc(a, ws, q0 + 16); cvt_load(da, ta, lane); }
;             if (v1) cvt_finish(db, tb, scr, lane);
;             if (v3) { db = conv_expert_desc(a, ws, q0 + 24); cvt_load(db, tb, lane); }
;             if (v2) cvt_finish(da, ta, scr, lane);
;             if (v3) cvt_finish(db, tb, scr, lane);
;         }
;         if (base >= (unsigned)target) break;
;         __syncthreads();
;     }
.LBB0_779:
	s_cmp_ge_u32 s35, s25
	s_mov_b64 s[0:1], -1
	s_cbranch_scc1 .LBB0_697
	s_add_i32 s30, s30, 1
	s_cmp_eq_u32 s30, 2
	s_cselect_b64 s[0:1], -1, 0
	s_barrier
	s_branch .LBB0_697
